# rowpass first-row prefetch issued at block-loop top (overlaps the parameter loads)
# baseline (speedup 1.0000x reference)
; DI float bflo(unsigned w) { return __uint_as_float(w << 16); }
; DI float bfhi(unsigned w) { return __uint_as_float(w & 0xffff0000u); }
; DI void ph_rowpass(const Frame& F) {
;     ...
;     for (int bi = F.wg; bi < M / 64; bi += F.nwg) {
;         const int blk = (F.nwg == 256) ? (((bi & 7) << 5) | (bi >> 3)) : bi;
;         const int bb = (blk * 64) >> 12; const float* mb = mod + (size_t)bb * 6 * D;
;         __syncthreads();
;         { const int d4 = F.tid; const f32x4 a = ((const f32x4*)gpm)[d4], g1 = ((const f32x4*)(mb + 2 * D))[d4] + ((const f32x4*)(mb + MOD_HALF + 2 * D))[d4], c = ((const f32x4*)gpf)[d4], sc = ((const f32x4*)(mb + 4 * D))[d4] + ((const f32x4*)(mb + MOD_HALF + 4 * D))[d4];
;           pgm[d4] = a * g1; pgf[d4] = c * (1.f + sc); psh[d4] = ((const f32x4*)(mb + 3 * D))[d4] + ((const f32x4*)(mb + MOD_HALF + 3 * D))[d4]; }
;         if ((blk & 63) == 0) { const int d4 = F.tid; ((f32x4*)((float*)(F.ws + WS_MOD) + 2 * MOD_HALF + (size_t)bb * D))[d4] = ((const f32x4*)(mb + 5 * D))[d4] + ((const f32x4*)(mb + MOD_HALF + 5 * D))[d4]; }
;         __syncthreads();
;       for (int m = blk * 64 + F.wave * 8; m < blk * 64 + F.wave * 8 + 8; ++m) {
;         const int b = m >> 12, s = m & 4095;
;         const u32x2* mr = (const u32x2*)(MIX + (size_t)m * D) + F.lane;
;         f32x4 v[8]; float ss = 0.f;
; #pragma unroll
;         for (int j = 0; j < 8; ++j) { const u32x2 w = __builtin_nontemporal_load(mr + 64 * j); v[j] = (f32x4){bflo(w.x), bfhi(w.x), bflo(w.y), bfhi(w.y)}; ss += (v[j][0] * v[j][0] + v[j][1] * v[j][1]) + (v[j][2] * v[j][2] + v[j][3] * v[j][3]); }
;         const f32x4* xr = (const f32x4*)(x + (size_t)m * D) + F.lane;
;         f32x4 xc[8];
; #pragma unroll
;         for (int j = 0; j < 8; ++j) xc[j] = __builtin_nontemporal_load(xr + 64 * j);
.LBB4_1118:
	s_lshl_b32 s10, s41, 5
	s_and_b32 s10, s10, 0xe0
	s_ashr_i32 s18, s41, 3
	s_or_b32 s10, s10, s18
	s_and_b64 s[18:19], s[12:13], exec
	s_cselect_b32 s10, s10, s41
	s_lshl_b32 s92, s10, 6
	s_add_i32 s92, s92, s30
	s_lshl_b32 s94, s92, 13
	s_mov_b32 s95, 0
	s_lshl_b32 s92, s92, 12
	s_mov_b32 s93, 0
	v_lshl_add_u64 v[252:253], v[52:53], 0, s[94:95]
	v_mov_b32_e32 v251, 0
	v_mov_b32_e32 v250, v54
	v_lshl_add_u64 v[250:251], v[250:251], 0, s[92:93]
	v_lshl_add_u64 v[250:251], v[250:251], 0, s[46:47]
	s_mov_b32 s92, 0x35800000
	s_nop 0
	v_lshl_add_u64 v[250:251], v[250:251], 0, s[92:93]
	global_load_dwordx2 v[218:219], v[250:251], off nt
	global_load_dwordx2 v[220:221], v[250:251], off offset:512 nt
	global_load_dwordx2 v[222:223], v[250:251], off offset:1024 nt
	global_load_dwordx2 v[224:225], v[250:251], off offset:1536 nt
	global_load_dwordx2 v[226:227], v[250:251], off offset:2048 nt
	global_load_dwordx2 v[228:229], v[250:251], off offset:2560 nt
	global_load_dwordx2 v[230:231], v[250:251], off offset:3072 nt
	global_load_dwordx2 v[232:233], v[250:251], off offset:3584 nt
	global_load_dwordx4 v[234:237], v[252:253], off nt
	global_load_dwordx4 v[238:241], v[252:253], off offset:1024 nt
	global_load_dwordx4 v[242:245], v[252:253], off offset:2048 nt
	global_load_dwordx4 v[246:249], v[252:253], off offset:3072 nt
	global_load_dword v254, v[250:251], off
	s_ashr_i32 s18, s10, 6
	s_mul_i32 s20, s18, 0xc000
	s_mul_hi_i32 s19, s18, 0xc000
	s_add_u32 s20, s28, s20
	s_addc_u32 s21, s29, s19
	v_lshl_add_u64 v[0:1], v[40:41], 4, s[20:21]
	v_add_co_u32_e32 v6, vcc, s24, v0
	s_nop 1
	v_addc_co_u32_e32 v7, vcc, 0, v1, vcc
	v_add_co_u32_e32 v10, vcc, s34, v0
	s_barrier
	s_nop 0
	v_addc_co_u32_e32 v11, vcc, 0, v1, vcc
	v_add_co_u32_e32 v14, vcc, s26, v0
	s_nop 1
	v_addc_co_u32_e32 v15, vcc, 0, v1, vcc
	v_add_co_u32_e32 v18, vcc, s35, v0
	global_load_dwordx4 v[2:5], v[42:43], off
	s_nop 0
	v_addc_co_u32_e32 v19, vcc, 0, v1, vcc
	v_add_co_u32_e32 v22, vcc, s25, v0
	global_load_dwordx4 v[6:9], v[6:7], off
	s_nop 0
	global_load_dwordx4 v[10:13], v[10:11], off
	v_addc_co_u32_e32 v23, vcc, 0, v1, vcc
	global_load_dwordx4 v[14:17], v[14:15], off
	s_nop 0
	global_load_dwordx4 v[18:21], v[18:19], off
	v_add_co_u32_e32 v26, vcc, s36, v0
	s_and_b32 s19, s10, 63
	s_nop 0
	v_addc_co_u32_e32 v27, vcc, 0, v1, vcc
	global_load_dwordx4 v[22:25], v[22:23], off
	s_nop 0
	global_load_dwordx4 v[26:29], v[26:27], off
	s_nop 0
	global_load_dwordx4 v[30:33], v[44:45], off
	s_cmp_lg_u32 s19, 0
	s_waitcnt vmcnt(5)
	v_pk_add_f32 v[8:9], v[8:9], v[12:13]
	v_pk_add_f32 v[6:7], v[6:7], v[10:11]
	v_pk_mul_f32 v[4:5], v[4:5], v[8:9]
	s_waitcnt vmcnt(3)
	v_pk_add_f32 v[10:11], v[16:17], v[20:21]
	v_pk_add_f32 v[12:13], v[14:15], v[18:19]
	v_pk_mul_f32 v[2:3], v[2:3], v[6:7]
	v_pk_add_f32 v[10:11], v[10:11], 1.0 op_sel_hi:[1,0]
	v_pk_add_f32 v[12:13], v[12:13], 1.0 op_sel_hi:[1,0]
	ds_write_b128 v51, v[2:5]
	s_waitcnt vmcnt(0)
	v_pk_mul_f32 v[4:5], v[32:33], v[10:11]
	v_pk_mul_f32 v[2:3], v[30:31], v[12:13]
	v_pk_add_f32 v[8:9], v[24:25], v[28:29]
	v_pk_add_f32 v[6:7], v[22:23], v[26:27]
	ds_write_b128 v55, v[2:5]
	ds_write_b128 v65, v[6:9]
	s_cbranch_scc1 .LBB4_1120
	v_add_co_u32_e32 v2, vcc, 0xa000, v0
	s_ashr_i32 s19, s18, 31
	s_nop 0
	v_addc_co_u32_e32 v3, vcc, 0, v1, vcc
	v_add_co_u32_e32 v4, vcc, 0x3a000, v0
	s_lshl_b64 s[18:19], s[18:19], 13
	s_nop 0
	v_addc_co_u32_e32 v5, vcc, 0, v1, vcc
	global_load_dwordx4 v[0:3], v[2:3], off
	s_nop 0
	global_load_dwordx4 v[4:7], v[4:5], off
	s_waitcnt vmcnt(0)
	v_pk_add_f32 v[2:3], v[2:3], v[6:7]
	v_pk_add_f32 v[0:1], v[0:1], v[4:5]
	v_lshl_add_u64 v[4:5], v[46:47], 0, s[18:19]
	global_store_dwordx4 v[4:5], v[0:3], off
